# P9 re-phasing variant: the second B half-tile (weights) instead of the A half-tile is the piece that moves one load interval later and is issued first there (waits 8/6/8/6)
# baseline (speedup 1.0000x reference)
; #define PG8_WAIT_VR() PG8_WAIT_V(8)
; template <class Epi, class Sched, bool F8 = false, bool PF = false, bool I8 = false, int PID = -1>
; __device__ __forceinline__ void gemm_phase(LAS unsigned char* lds, LAS unsigned char* xlds, const int RP, const int RPB, const int nt, const Sched& S, const Epi& E, const int stagger_ticks) {
;     ...
;         for (int t = 0; t < nt; t += 2) {
;             const bool last = (t == nt - 2);
;             unsigned ldsb = ldsb0; asm volatile("" : "+s"(ldsb));
;             const char* a1 = cA + (size_t)(t + 1) * kstep;
;             const char* a2 = last ? nA : cA + (size_t)(t + 2) * kstep; const char* b2 = last ? nB : cB + (size_t)(t + 2) * kstep;
;             const char* a3 = a2 + kstep; const char* b3 = b2 + kstep;
;             if constexpr (PF) { const char* pfa = (t + 4 < nt) ? cA + (size_t)(t + 4) * kstep : nA + (size_t)(t + 4 - nt) * kstep;
;                 asm volatile("s_mov_b32 m0, %2\n\ts_nop 0\n\tglobal_load_lds_dword %0, %1" :: "v"(voffP), "s"(pfa), "s"(ldsP) : "memory", "m0"); }
;             const bool relax = (Epi::RELAX > 0) && (t == 0) && epi_ran;
;             PG8_LDB(B0, 0, 0); PG8_LDB(B1, 0, 1); PG8_SCHED; PG8_LDA(At, 0, 0); PG8_STAGEA1(PG8_SA(1, 1), a1);
;             if (Sched::GATHER) { if (last) { const u32x4 nv = *nslot; vA0 = nv.x; vA1 = nv.y; vA2 = nv.z; vA3 = nv.w; } }
;             PG8_WAIT_VX(); PG8_WAIT_L(0); PG8_BAR; PG8_MMA(0, 0, At, B0); PG8_MMA(0, 1, At, B1); PG8_BAR; PG8_SCHED;
;             if constexpr (Epi::BIAS_DMA) { if (t == 0 && has_next) E.bias_dma(nxt, xlds + 8192 + ((ui + 1) & 1) * Epi::BIAS_STRIDE, wid, lane); }
;             PG8_LDA(At, 0, 1); PG8_STAGE(PG8_SB(0, 0), b2, voffB); PG8_STAGE(PG8_SB(0, 1), b2 + hstepB, voffB); PG8_STAGEA(PG8_SA(0, 0), a2, vA0, vA1);
;             PG8_WAIT_VX(); PG8_WAIT_L(0); PG8_BAR; PG8_MMA(1, 0, At, B0); PG8_MMA(1, 1, At, B1); PG8_BAR; PG8_SCHED;
;             PG8_LDB(B0, 1, 0); PG8_LDB(B1, 1, 1); PG8_SCHED; PG8_LDA(At, 1, 0); PG8_STAGEA1(PG8_SA(0, 1), a2);
;             PG8_WAIT_VR(); PG8_WAIT_L(0); PG8_BAR; PG8_MMA(0, 0, At, B0); PG8_MMA(0, 1, At, B1); PG8_BAR; PG8_SCHED;
;             PG8_LDA(At, 1, 1); PG8_STAGE(PG8_SB(1, 0), b3, voffB); PG8_STAGE(PG8_SB(1, 1), b3 + hstepB, voffB); PG8_STAGEA(PG8_SA(1, 0), a3, vA0, vA1);
;             PG8_WAIT_VR(); PG8_WAIT_L(0); PG8_BAR; PG8_MMA(1, 0, At, B0); PG8_MMA(1, 1, At, B1); PG8_BAR; PG8_SCHED;
.LBB0_1062:
	s_add_u32 s30, s26, 0xfffe0080
	s_addc_u32 s31, s27, -1
	s_cmp_eq_u32 s73, 4
	s_cselect_b32 s38, s6, s30
	s_cselect_b32 s39, s7, s31
	s_cselect_b32 s34, s8, s25
	s_cselect_b32 s35, s9, s71
	s_add_u32 s30, s38, 0x80
	s_addc_u32 s31, s39, 0
	s_add_u32 s36, s34, 0x80
	s_addc_u32 s37, s35, 0
	ds_read_b128 v[170:173], v169 offset:16384
	ds_read_b128 v[174:177], v169 offset:17408
	ds_read_b128 v[178:181], v169 offset:18432
	ds_read_b128 v[182:185], v169 offset:19456
	ds_read_b128 v[186:189], v169 offset:20480
	ds_read_b128 v[190:193], v169 offset:21504
	ds_read_b128 v[194:197], v169 offset:22528
	ds_read_b128 v[198:201], v169 offset:23552
	s_add_i32 s75, s74, 0x10000
	s_mov_b32 m0, s75
	s_nop 0
	global_load_lds_dwordx4 v166, s[34:35]
	s_add_i32 s75, s74, 0x12000
	s_mov_b32 m0, s75
	s_nop 0
	global_load_lds_dwordx4 v167, s[34:35]
	s_add_i32 s75, s74, 0x2000
	s_mov_b32 m0, s74
	s_nop 0
	global_load_lds_dwordx4 v164, s[38:39]
	s_nop 0
	s_mov_b32 m0, s75
	s_nop 0
	global_load_lds_dwordx4 v165, s[38:39]
	s_waitcnt vmcnt(6)
	s_waitcnt lgkmcnt(0)
	s_barrier
	s_setprio 1
	s_waitcnt lgkmcnt(6)
	v_mfma_f32_16x16x128_f8f6f4 v[86:89], v[2:9], v[170:177], v[86:89]
	v_mfma_f32_16x16x128_f8f6f4 v[82:85], v[10:17], v[170:177], v[82:85]
	s_waitcnt lgkmcnt(4)
	v_mfma_f32_16x16x128_f8f6f4 v[70:73], v[2:9], v[178:185], v[70:73]
	v_mfma_f32_16x16x128_f8f6f4 v[66:69], v[10:17], v[178:185], v[66:69]
	s_waitcnt lgkmcnt(2)
	v_mfma_f32_16x16x128_f8f6f4 v[202:205], v[2:9], v[186:193], v[54:57]
	v_mfma_f32_16x16x128_f8f6f4 v[206:209], v[10:17], v[186:193], v[50:53]
	s_waitcnt lgkmcnt(0)
	v_mfma_f32_16x16x128_f8f6f4 v[210:213], v[2:9], v[194:201], v[38:41]
	v_mfma_f32_16x16x128_f8f6f4 v[214:217], v[10:17], v[194:201], v[34:37]
	v_mfma_f32_16x16x128_f8f6f4 v[94:97], v[18:25], v[170:177], v[94:97]
	v_mfma_f32_16x16x128_f8f6f4 v[90:93], v[26:33], v[170:177], v[90:93]
	v_mfma_f32_16x16x128_f8f6f4 v[78:81], v[18:25], v[178:185], v[78:81]
	v_mfma_f32_16x16x128_f8f6f4 v[74:77], v[26:33], v[178:185], v[74:77]
	v_mfma_f32_16x16x128_f8f6f4 v[218:221], v[18:25], v[186:193], v[62:65]
	v_mfma_f32_16x16x128_f8f6f4 v[186:189], v[26:33], v[186:193], v[58:61]
	v_mfma_f32_16x16x128_f8f6f4 v[190:193], v[18:25], v[194:201], v[46:49]
	v_mfma_f32_16x16x128_f8f6f4 v[194:197], v[26:33], v[194:201], v[42:45]
	s_setprio 0
	s_barrier
	v_add_u32_e32 v14, 0x18000, v168
	v_add_u32_e32 v30, 0x1c000, v168
	ds_read_b128 v[2:5], v14
	ds_read_b128 v[6:9], v14 offset:1024
	ds_read_b128 v[10:13], v14 offset:2048
	ds_read_b128 v[14:17], v14 offset:3072
	ds_read_b128 v[18:21], v30
	ds_read_b128 v[22:25], v30 offset:1024
	ds_read_b128 v[26:29], v30 offset:2048
	ds_read_b128 v[30:33], v30 offset:3072
	ds_read_b128 v[34:37], v169 offset:32768
	ds_read_b128 v[38:41], v169 offset:33792
	ds_read_b128 v[42:45], v169 offset:34816
	ds_read_b128 v[46:49], v169 offset:35840
	ds_read_b128 v[50:53], v169 offset:36864
	ds_read_b128 v[54:57], v169 offset:37888
	ds_read_b128 v[58:61], v169 offset:38912
	ds_read_b128 v[62:65], v169 offset:39936
	s_add_u32 s76, s34, 0x2000
	s_addc_u32 s77, s35, 0
	s_add_i32 s75, s74, 0x14000
	s_mov_b32 m0, s75
	s_nop 0
	global_load_lds_dwordx4 v166, s[76:77]
	s_add_i32 s75, s74, 0x16000
	s_mov_b32 m0, s75
	s_nop 0
	global_load_lds_dwordx4 v167, s[76:77]
	s_add_u32 s38, s38, 0x20000
	s_addc_u32 s39, s39, 0
	s_add_i32 s75, s74, 0x4000
	s_mov_b32 m0, s75
	s_nop 0
	global_load_lds_dwordx4 v164, s[38:39]
	s_add_i32 s75, s74, 0x6000
	s_mov_b32 m0, s75
	s_nop 0
	global_load_lds_dwordx4 v165, s[38:39]
	s_waitcnt vmcnt(8)
	s_waitcnt lgkmcnt(0)
	s_barrier
	s_setprio 1
	s_waitcnt lgkmcnt(6)
	v_mfma_f32_16x16x128_f8f6f4 v[150:153], v[2:9], v[34:41], v[150:153]
	v_mfma_f32_16x16x128_f8f6f4 v[146:149], v[10:17], v[34:41], v[146:149]
	s_waitcnt lgkmcnt(4)
	v_mfma_f32_16x16x128_f8f6f4 v[134:137], v[2:9], v[42:49], v[134:137]
	v_mfma_f32_16x16x128_f8f6f4 v[130:133], v[10:17], v[42:49], v[130:133]
	s_waitcnt lgkmcnt(2)
	v_mfma_f32_16x16x128_f8f6f4 v[118:121], v[2:9], v[50:57], v[118:121]
	v_mfma_f32_16x16x128_f8f6f4 v[114:117], v[10:17], v[50:57], v[114:117]
	s_waitcnt lgkmcnt(0)
	v_mfma_f32_16x16x128_f8f6f4 v[102:105], v[2:9], v[58:65], v[102:105]
	v_mfma_f32_16x16x128_f8f6f4 v[98:101], v[10:17], v[58:65], v[98:101]
	v_mfma_f32_16x16x128_f8f6f4 v[158:161], v[18:25], v[34:41], v[158:161]
	v_mfma_f32_16x16x128_f8f6f4 v[154:157], v[26:33], v[34:41], v[154:157]
	v_mfma_f32_16x16x128_f8f6f4 v[142:145], v[18:25], v[42:49], v[142:145]
	v_mfma_f32_16x16x128_f8f6f4 v[138:141], v[26:33], v[42:49], v[138:141]
	v_mfma_f32_16x16x128_f8f6f4 v[126:129], v[18:25], v[50:57], v[126:129]
	v_mfma_f32_16x16x128_f8f6f4 v[122:125], v[26:33], v[50:57], v[122:125]
	v_mfma_f32_16x16x128_f8f6f4 v[110:113], v[18:25], v[58:65], v[110:113]
	v_mfma_f32_16x16x128_f8f6f4 v[106:109], v[26:33], v[58:65], v[106:109]
	s_setprio 0
	s_barrier
	ds_read_b128 v[42:45], v169 offset:49152
	ds_read_b128 v[46:49], v169 offset:50176
	ds_read_b128 v[58:61], v169 offset:51200
	ds_read_b128 v[62:65], v169 offset:52224
	ds_read_b128 v[170:173], v169 offset:53248
	ds_read_b128 v[174:177], v169 offset:54272
	ds_read_b128 v[178:181], v169 offset:55296
	ds_read_b128 v[182:185], v169 offset:56320
	s_add_i32 s38, s74, 0x18000
	s_mov_b32 m0, s38
	s_nop 0
	global_load_lds_dwordx4 v166, s[36:37]
	s_add_i32 s38, s74, 0x1a000
	s_mov_b32 m0, s38
	s_nop 0
	global_load_lds_dwordx4 v167, s[36:37]
	s_add_i32 s34, s74, 0x8000
	s_mov_b32 m0, s34
	s_nop 0
	global_load_lds_dwordx4 v164, s[30:31]
	s_add_i32 s74, s74, 0xa000
	s_mov_b32 m0, s74
	s_nop 0
	global_load_lds_dwordx4 v165, s[30:31]
	s_waitcnt vmcnt(6)
	s_waitcnt lgkmcnt(0)
	s_barrier
	s_setprio 1
	s_waitcnt lgkmcnt(6)
	v_mfma_f32_16x16x128_f8f6f4 v[86:89], v[2:9], v[42:49], v[86:89]
	v_mfma_f32_16x16x128_f8f6f4 v[82:85], v[10:17], v[42:49], v[82:85]
	s_waitcnt lgkmcnt(4)
	v_mfma_f32_16x16x128_f8f6f4 v[70:73], v[2:9], v[58:65], v[70:73]
	v_mfma_f32_16x16x128_f8f6f4 v[66:69], v[10:17], v[58:65], v[66:69]
	s_waitcnt lgkmcnt(2)
	v_mfma_f32_16x16x128_f8f6f4 v[54:57], v[2:9], v[170:177], v[202:205]
	v_mfma_f32_16x16x128_f8f6f4 v[50:53], v[10:17], v[170:177], v[206:209]
	s_waitcnt lgkmcnt(0)
	v_mfma_f32_16x16x128_f8f6f4 v[38:41], v[2:9], v[178:185], v[210:213]
	v_mfma_f32_16x16x128_f8f6f4 v[34:37], v[10:17], v[178:185], v[214:217]
	v_mfma_f32_16x16x128_f8f6f4 v[94:97], v[18:25], v[42:49], v[94:97]
	v_mfma_f32_16x16x128_f8f6f4 v[90:93], v[26:33], v[42:49], v[90:93]
	v_mfma_f32_16x16x128_f8f6f4 v[78:81], v[18:25], v[58:65], v[78:81]
	v_mfma_f32_16x16x128_f8f6f4 v[74:77], v[26:33], v[58:65], v[74:77]
	v_mfma_f32_16x16x128_f8f6f4 v[62:65], v[18:25], v[170:177], v[218:221]
	v_mfma_f32_16x16x128_f8f6f4 v[58:61], v[26:33], v[170:177], v[186:189]
	v_mfma_f32_16x16x128_f8f6f4 v[46:49], v[18:25], v[178:185], v[190:193]
	v_mfma_f32_16x16x128_f8f6f4 v[42:45], v[26:33], v[178:185], v[194:197]
	s_setprio 0
	s_barrier
	s_add_i32 s73, s73, 2
	s_add_u32 s25, s25, 0x100
	s_addc_u32 s71, s71, 0
	s_add_u32 s26, s26, 0x100
	s_addc_u32 s27, s27, 0
	s_cmp_gt_u32 s73, 5
	s_cbranch_scc1 .LBB0_1065
; #define PG8_WAIT_VR() PG8_WAIT_V(8)
; template <class Epi, class Sched, bool F8 = false, bool PF = false, bool I8 = false, int PID = -1>
; __device__ __forceinline__ void gemm_phase(LAS unsigned char* lds, LAS unsigned char* xlds, const int RP, const int RPB, const int nt, const Sched& S, const Epi& E, const int stagger_ticks) {
;     ...
;         for (int t = 0; t < nt; t += 2) {
;             const bool last = (t == nt - 2);
;             unsigned ldsb = ldsb0; asm volatile("" : "+s"(ldsb));
;             const char* a1 = cA + (size_t)(t + 1) * kstep;
;             const char* a2 = last ? nA : cA + (size_t)(t + 2) * kstep; const char* b2 = last ? nB : cB + (size_t)(t + 2) * kstep;
;             const char* a3 = a2 + kstep; const char* b3 = b2 + kstep;
;             if constexpr (PF) { const char* pfa = (t + 4 < nt) ? cA + (size_t)(t + 4) * kstep : nA + (size_t)(t + 4 - nt) * kstep;
;                 asm volatile("s_mov_b32 m0, %2\n\ts_nop 0\n\tglobal_load_lds_dword %0, %1" :: "v"(voffP), "s"(pfa), "s"(ldsP) : "memory", "m0"); }
;             const bool relax = (Epi::RELAX > 0) && (t == 0) && epi_ran;
;             PG8_LDB(B0, 0, 0); PG8_LDB(B1, 0, 1); PG8_SCHED; PG8_LDA(At, 0, 0); PG8_STAGEA1(PG8_SA(1, 1), a1);
;             if (Sched::GATHER) { if (last) { const u32x4 nv = *nslot; vA0 = nv.x; vA1 = nv.y; vA2 = nv.z; vA3 = nv.w; } }
;             PG8_WAIT_VX(); PG8_WAIT_L(0); PG8_BAR; PG8_MMA(0, 0, At, B0); PG8_MMA(0, 1, At, B1); PG8_BAR; PG8_SCHED;
;             if constexpr (Epi::BIAS_DMA) { if (t == 0 && has_next) E.bias_dma(nxt, xlds + 8192 + ((ui + 1) & 1) * Epi::BIAS_STRIDE, wid, lane); }
;             PG8_LDA(At, 0, 1); PG8_STAGE(PG8_SB(0, 0), b2, voffB); PG8_STAGE(PG8_SB(0, 1), b2 + hstepB, voffB); PG8_STAGEA(PG8_SA(0, 0), a2, vA0, vA1);
;             PG8_WAIT_VX(); PG8_WAIT_L(0); PG8_BAR; PG8_MMA(1, 0, At, B0); PG8_MMA(1, 1, At, B1); PG8_BAR; PG8_SCHED;
;             PG8_LDB(B0, 1, 0); PG8_LDB(B1, 1, 1); PG8_SCHED; PG8_LDA(At, 1, 0); PG8_STAGEA1(PG8_SA(0, 1), a2);
;             PG8_WAIT_VR(); PG8_WAIT_L(0); PG8_BAR; PG8_MMA(0, 0, At, B0); PG8_MMA(0, 1, At, B1); PG8_BAR; PG8_SCHED;
;             PG8_LDA(At, 1, 1); PG8_STAGE(PG8_SB(1, 0), b3, voffB); PG8_STAGE(PG8_SB(1, 1), b3 + hstepB, voffB); PG8_STAGEA(PG8_SA(1, 0), a3, vA0, vA1);
;             PG8_WAIT_VR(); PG8_WAIT_L(0); PG8_BAR; PG8_MMA(1, 0, At, B0); PG8_MMA(1, 1, At, B1); PG8_BAR; PG8_SCHED;
.LBB0_1063:
	s_mov_b32 s74, s47
	v_add_u32_e32 v14, 0x10000, v168
	v_add_u32_e32 v30, 0x14000, v168
	ds_read_b128 v[2:5], v14
	ds_read_b128 v[6:9], v14 offset:1024
	ds_read_b128 v[10:13], v14 offset:2048
	ds_read_b128 v[14:17], v14 offset:3072
	ds_read_b128 v[18:21], v30
	ds_read_b128 v[22:25], v30 offset:1024
	ds_read_b128 v[26:29], v30 offset:2048
	ds_read_b128 v[30:33], v30 offset:3072
	ds_read_b128 v[170:173], v169
	ds_read_b128 v[174:177], v169 offset:1024
	ds_read_b128 v[178:181], v169 offset:2048
	ds_read_b128 v[182:185], v169 offset:3072
	ds_read_b128 v[186:189], v169 offset:4096
	ds_read_b128 v[190:193], v169 offset:5120
	ds_read_b128 v[194:197], v169 offset:6144
	ds_read_b128 v[198:201], v169 offset:7168
	s_add_u32 s100, s25, 0x1f80
	s_addc_u32 s101, s71, 0
	s_add_i32 s30, s74, 0x1c000
	s_mov_b32 m0, s30
	s_nop 0
	global_load_lds_dwordx4 v166, s[100:101]
	s_add_i32 s30, s74, 0x1e000
	s_mov_b32 m0, s30
	s_nop 0
	global_load_lds_dwordx4 v167, s[100:101]
	s_add_i32 s30, s74, 0xc000
	s_mov_b32 m0, s30
	s_nop 0
	global_load_lds_dwordx4 v164, s[26:27]
	s_add_i32 s30, s74, 0xe000
	s_mov_b32 m0, s30
	s_nop 0
	global_load_lds_dwordx4 v165, s[26:27]
	s_waitcnt vmcnt(8)
	s_waitcnt lgkmcnt(0)
	s_barrier
	s_setprio 1
	s_waitcnt lgkmcnt(6)
	v_mfma_f32_16x16x128_f8f6f4 v[150:153], v[2:9], v[170:177], v[150:153]
	v_mfma_f32_16x16x128_f8f6f4 v[146:149], v[10:17], v[170:177], v[146:149]
	s_waitcnt lgkmcnt(4)
	v_mfma_f32_16x16x128_f8f6f4 v[134:137], v[2:9], v[178:185], v[134:137]
	v_mfma_f32_16x16x128_f8f6f4 v[130:133], v[10:17], v[178:185], v[130:133]
	s_waitcnt lgkmcnt(2)
	v_mfma_f32_16x16x128_f8f6f4 v[118:121], v[2:9], v[186:193], v[118:121]
	v_mfma_f32_16x16x128_f8f6f4 v[114:117], v[10:17], v[186:193], v[114:117]
	s_waitcnt lgkmcnt(0)
	v_mfma_f32_16x16x128_f8f6f4 v[102:105], v[2:9], v[194:201], v[102:105]
	v_mfma_f32_16x16x128_f8f6f4 v[98:101], v[10:17], v[194:201], v[98:101]
	v_mfma_f32_16x16x128_f8f6f4 v[158:161], v[18:25], v[170:177], v[158:161]
	v_mfma_f32_16x16x128_f8f6f4 v[154:157], v[26:33], v[170:177], v[154:157]
	v_mfma_f32_16x16x128_f8f6f4 v[142:145], v[18:25], v[178:185], v[142:145]
	v_mfma_f32_16x16x128_f8f6f4 v[138:141], v[26:33], v[178:185], v[138:141]
	v_mfma_f32_16x16x128_f8f6f4 v[126:129], v[18:25], v[186:193], v[126:129]
	v_mfma_f32_16x16x128_f8f6f4 v[122:125], v[26:33], v[186:193], v[122:125]
	v_mfma_f32_16x16x128_f8f6f4 v[110:113], v[18:25], v[194:201], v[110:113]
	v_mfma_f32_16x16x128_f8f6f4 v[106:109], v[26:33], v[194:201], v[106:109]
	s_setprio 0
	s_barrier
	s_cmp_lg_u32 s73, -2
	s_cselect_b64 s[30:31], -1, 0
	s_or_b64 s[30:31], s[30:31], s[28:29]
	s_and_b64 vcc, exec, s[30:31]
	s_cbranch_vccnz .LBB0_1062
	s_mov_b32 m0, s72
	s_nop 0
	global_load_lds_dword v1, s[2:3]
	s_branch .LBB0_1062
.Lmy_z8t:
	s_mov_b32 s74, s47
	v_add_u32_e32 v14, 0x10000, v168
	v_add_u32_e32 v30, 0x14000, v168
	ds_read_b128 v[2:5], v14
	ds_read_b128 v[6:9], v14 offset:1024
	ds_read_b128 v[10:13], v14 offset:2048
	ds_read_b128 v[14:17], v14 offset:3072
	ds_read_b128 v[18:21], v30
	ds_read_b128 v[22:25], v30 offset:1024
	ds_read_b128 v[26:29], v30 offset:2048
	ds_read_b128 v[30:33], v30 offset:3072
	ds_read_b128 v[170:173], v169
	ds_read_b128 v[174:177], v169 offset:1024
	ds_read_b128 v[178:181], v169 offset:2048
	ds_read_b128 v[182:185], v169 offset:3072
	ds_read_b128 v[186:189], v169 offset:4096
	ds_read_b128 v[190:193], v169 offset:5120
	ds_read_b128 v[194:197], v169 offset:6144
	ds_read_b128 v[198:201], v169 offset:7168
	s_add_u32 s100, s25, 0x1f80
	s_addc_u32 s101, s71, 0
	s_add_i32 s30, s74, 0x1c000
	s_mov_b32 m0, s30
	s_nop 0
	global_load_lds_dwordx4 v166, s[100:101]
	s_add_i32 s30, s74, 0x1e000
	s_mov_b32 m0, s30
	s_nop 0
	global_load_lds_dwordx4 v167, s[100:101]
	s_add_i32 s30, s74, 0xc000
	s_mov_b32 m0, s30
	s_nop 0
	global_load_lds_dwordx4 v164, s[26:27]
	s_add_i32 s30, s74, 0xe000
	s_mov_b32 m0, s30
	s_nop 0
	global_load_lds_dwordx4 v165, s[26:27]
	s_waitcnt vmcnt(8)
	s_waitcnt lgkmcnt(0)
	s_barrier
	s_setprio 1
	s_waitcnt lgkmcnt(6)
	v_mfma_f32_16x16x128_f8f6f4 v[150:153], v[2:9], v[170:177], 0
	v_mfma_f32_16x16x128_f8f6f4 v[146:149], v[10:17], v[170:177], 0
	s_waitcnt lgkmcnt(4)
	v_mfma_f32_16x16x128_f8f6f4 v[134:137], v[2:9], v[178:185], 0
	v_mfma_f32_16x16x128_f8f6f4 v[130:133], v[10:17], v[178:185], 0
	s_waitcnt lgkmcnt(2)
	v_mfma_f32_16x16x128_f8f6f4 v[118:121], v[2:9], v[186:193], 0
	v_mfma_f32_16x16x128_f8f6f4 v[114:117], v[10:17], v[186:193], 0
	s_waitcnt lgkmcnt(0)
	v_mfma_f32_16x16x128_f8f6f4 v[102:105], v[2:9], v[194:201], 0
	v_mfma_f32_16x16x128_f8f6f4 v[98:101], v[10:17], v[194:201], 0
	v_mfma_f32_16x16x128_f8f6f4 v[158:161], v[18:25], v[170:177], 0
	v_mfma_f32_16x16x128_f8f6f4 v[154:157], v[26:33], v[170:177], 0
	v_mfma_f32_16x16x128_f8f6f4 v[142:145], v[18:25], v[178:185], 0
	v_mfma_f32_16x16x128_f8f6f4 v[138:141], v[26:33], v[178:185], 0
	v_mfma_f32_16x16x128_f8f6f4 v[126:129], v[18:25], v[186:193], 0
	v_mfma_f32_16x16x128_f8f6f4 v[122:125], v[26:33], v[186:193], 0
	v_mfma_f32_16x16x128_f8f6f4 v[110:113], v[18:25], v[194:201], 0
	v_mfma_f32_16x16x128_f8f6f4 v[106:109], v[26:33], v[194:201], 0
	s_setprio 0
	s_barrier
	s_cmp_lg_u32 s73, -2
	s_cselect_b64 s[30:31], -1, 0
	s_or_b64 s[30:31], s[30:31], s[28:29]
	s_and_b64 vcc, exec, s[30:31]
	s_cbranch_vccnz .Lmy_z8b
	s_mov_b32 m0, s72
	s_nop 0
	global_load_lds_dword v1, s[2:3]
	s_branch .Lmy_z8b
; #define PG8_WAIT_VR() PG8_WAIT_V(8)
; template <class Epi, class Sched, bool F8 = false, bool PF = false, bool I8 = false, int PID = -1>
; __device__ __forceinline__ void gemm_phase(LAS unsigned char* lds, LAS unsigned char* xlds, const int RP, const int RPB, const int nt, const Sched& S, const Epi& E, const int stagger_ticks) {
;     ...
;         for (int t = 0; t < nt; t += 2) {
;             const bool last = (t == nt - 2);
;             unsigned ldsb = ldsb0; asm volatile("" : "+s"(ldsb));
;             const char* a1 = cA + (size_t)(t + 1) * kstep;
;             const char* a2 = last ? nA : cA + (size_t)(t + 2) * kstep; const char* b2 = last ? nB : cB + (size_t)(t + 2) * kstep;
;             const char* a3 = a2 + kstep; const char* b3 = b2 + kstep;
;             if constexpr (PF) { const char* pfa = (t + 4 < nt) ? cA + (size_t)(t + 4) * kstep : nA + (size_t)(t + 4 - nt) * kstep;
;                 asm volatile("s_mov_b32 m0, %2\n\ts_nop 0\n\tglobal_load_lds_dword %0, %1" :: "v"(voffP), "s"(pfa), "s"(ldsP) : "memory", "m0"); }
;             const bool relax = (Epi::RELAX > 0) && (t == 0) && epi_ran;
;             PG8_LDB(B0, 0, 0); PG8_LDB(B1, 0, 1); PG8_SCHED; PG8_LDA(At, 0, 0); PG8_STAGEA1(PG8_SA(1, 1), a1);
;             if (Sched::GATHER) { if (last) { const u32x4 nv = *nslot; vA0 = nv.x; vA1 = nv.y; vA2 = nv.z; vA3 = nv.w; } }
;             PG8_WAIT_VX(); PG8_WAIT_L(0); PG8_BAR; PG8_MMA(0, 0, At, B0); PG8_MMA(0, 1, At, B1); PG8_BAR; PG8_SCHED;
;             if constexpr (Epi::BIAS_DMA) { if (t == 0 && has_next) E.bias_dma(nxt, xlds + 8192 + ((ui + 1) & 1) * Epi::BIAS_STRIDE, wid, lane); }
;             PG8_LDA(At, 0, 1); PG8_STAGE(PG8_SB(0, 0), b2, voffB); PG8_STAGE(PG8_SB(0, 1), b2 + hstepB, voffB); PG8_STAGEA(PG8_SA(0, 0), a2, vA0, vA1);
;             PG8_WAIT_VX(); PG8_WAIT_L(0); PG8_BAR; PG8_MMA(1, 0, At, B0); PG8_MMA(1, 1, At, B1); PG8_BAR; PG8_SCHED;
;             PG8_LDB(B0, 1, 0); PG8_LDB(B1, 1, 1); PG8_SCHED; PG8_LDA(At, 1, 0); PG8_STAGEA1(PG8_SA(0, 1), a2);
;             PG8_WAIT_VR(); PG8_WAIT_L(0); PG8_BAR; PG8_MMA(0, 0, At, B0); PG8_MMA(0, 1, At, B1); PG8_BAR; PG8_SCHED;
;             PG8_LDA(At, 1, 1); PG8_STAGE(PG8_SB(1, 0), b3, voffB); PG8_STAGE(PG8_SB(1, 1), b3 + hstepB, voffB); PG8_STAGEA(PG8_SA(1, 0), a3, vA0, vA1);
;             PG8_WAIT_VR(); PG8_WAIT_L(0); PG8_BAR; PG8_MMA(1, 0, At, B0); PG8_MMA(1, 1, At, B1); PG8_BAR; PG8_SCHED;
.Lmy_z8b:
	s_add_u32 s30, s26, 0xfffe0080
	s_addc_u32 s31, s27, -1
	s_cmp_eq_u32 s73, 4
	s_cselect_b32 s38, s6, s30
	s_cselect_b32 s39, s7, s31
	s_cselect_b32 s34, s8, s25
	s_cselect_b32 s35, s9, s71
	s_add_u32 s30, s38, 0x80
	s_addc_u32 s31, s39, 0
	s_add_u32 s36, s34, 0x80
	s_addc_u32 s37, s35, 0
	ds_read_b128 v[170:173], v169 offset:16384
	ds_read_b128 v[174:177], v169 offset:17408
	ds_read_b128 v[178:181], v169 offset:18432
	ds_read_b128 v[182:185], v169 offset:19456
	ds_read_b128 v[186:189], v169 offset:20480
	ds_read_b128 v[190:193], v169 offset:21504
	ds_read_b128 v[194:197], v169 offset:22528
	ds_read_b128 v[198:201], v169 offset:23552
	s_add_i32 s75, s74, 0x10000
	s_mov_b32 m0, s75
	s_nop 0
	global_load_lds_dwordx4 v166, s[34:35]
	s_add_i32 s75, s74, 0x12000
	s_mov_b32 m0, s75
	s_nop 0
	global_load_lds_dwordx4 v167, s[34:35]
	s_add_i32 s75, s74, 0x2000
	s_mov_b32 m0, s74
	s_nop 0
	global_load_lds_dwordx4 v164, s[38:39]
	s_nop 0
	s_mov_b32 m0, s75
	s_nop 0
	global_load_lds_dwordx4 v165, s[38:39]
	s_waitcnt vmcnt(6)
	s_waitcnt lgkmcnt(0)
	s_barrier
	s_setprio 1
	s_waitcnt lgkmcnt(6)
	v_mfma_f32_16x16x128_f8f6f4 v[86:89], v[2:9], v[170:177], 0
	v_mfma_f32_16x16x128_f8f6f4 v[82:85], v[10:17], v[170:177], 0
	s_waitcnt lgkmcnt(4)
	v_mfma_f32_16x16x128_f8f6f4 v[70:73], v[2:9], v[178:185], 0
	v_mfma_f32_16x16x128_f8f6f4 v[66:69], v[10:17], v[178:185], 0
	s_waitcnt lgkmcnt(2)
	v_mfma_f32_16x16x128_f8f6f4 v[202:205], v[2:9], v[186:193], 0
	v_mfma_f32_16x16x128_f8f6f4 v[206:209], v[10:17], v[186:193], 0
	s_waitcnt lgkmcnt(0)
	v_mfma_f32_16x16x128_f8f6f4 v[210:213], v[2:9], v[194:201], 0
	v_mfma_f32_16x16x128_f8f6f4 v[214:217], v[10:17], v[194:201], 0
	v_mfma_f32_16x16x128_f8f6f4 v[94:97], v[18:25], v[170:177], 0
	v_mfma_f32_16x16x128_f8f6f4 v[90:93], v[26:33], v[170:177], 0
	v_mfma_f32_16x16x128_f8f6f4 v[78:81], v[18:25], v[178:185], 0
	v_mfma_f32_16x16x128_f8f6f4 v[74:77], v[26:33], v[178:185], 0
	v_mfma_f32_16x16x128_f8f6f4 v[218:221], v[18:25], v[186:193], 0
	v_mfma_f32_16x16x128_f8f6f4 v[186:189], v[26:33], v[186:193], 0
	v_mfma_f32_16x16x128_f8f6f4 v[190:193], v[18:25], v[194:201], 0
	v_mfma_f32_16x16x128_f8f6f4 v[194:197], v[26:33], v[194:201], 0
	s_setprio 0
	s_barrier
	v_add_u32_e32 v14, 0x18000, v168
	v_add_u32_e32 v30, 0x1c000, v168
	ds_read_b128 v[2:5], v14
	ds_read_b128 v[6:9], v14 offset:1024
	ds_read_b128 v[10:13], v14 offset:2048
	ds_read_b128 v[14:17], v14 offset:3072
	ds_read_b128 v[18:21], v30
	ds_read_b128 v[22:25], v30 offset:1024
	ds_read_b128 v[26:29], v30 offset:2048
	ds_read_b128 v[30:33], v30 offset:3072
	ds_read_b128 v[34:37], v169 offset:32768
	ds_read_b128 v[38:41], v169 offset:33792
	ds_read_b128 v[42:45], v169 offset:34816
	ds_read_b128 v[46:49], v169 offset:35840
	ds_read_b128 v[50:53], v169 offset:36864
	ds_read_b128 v[54:57], v169 offset:37888
	ds_read_b128 v[58:61], v169 offset:38912
	ds_read_b128 v[62:65], v169 offset:39936
	s_add_u32 s76, s34, 0x2000
	s_addc_u32 s77, s35, 0
	s_add_i32 s75, s74, 0x14000
	s_mov_b32 m0, s75
	s_nop 0
	global_load_lds_dwordx4 v166, s[76:77]
	s_add_i32 s75, s74, 0x16000
	s_mov_b32 m0, s75
	s_nop 0
	global_load_lds_dwordx4 v167, s[76:77]
	s_add_u32 s38, s38, 0x20000
	s_addc_u32 s39, s39, 0
	s_add_i32 s75, s74, 0x4000
	s_mov_b32 m0, s75
	s_nop 0
	global_load_lds_dwordx4 v164, s[38:39]
	s_add_i32 s75, s74, 0x6000
	s_mov_b32 m0, s75
	s_nop 0
	global_load_lds_dwordx4 v165, s[38:39]
	s_waitcnt vmcnt(8)
	s_waitcnt lgkmcnt(0)
	s_barrier
	s_setprio 1
	s_waitcnt lgkmcnt(6)
	v_mfma_f32_16x16x128_f8f6f4 v[150:153], v[2:9], v[34:41], v[150:153]
	v_mfma_f32_16x16x128_f8f6f4 v[146:149], v[10:17], v[34:41], v[146:149]
	s_waitcnt lgkmcnt(4)
	v_mfma_f32_16x16x128_f8f6f4 v[134:137], v[2:9], v[42:49], v[134:137]
	v_mfma_f32_16x16x128_f8f6f4 v[130:133], v[10:17], v[42:49], v[130:133]
	s_waitcnt lgkmcnt(2)
	v_mfma_f32_16x16x128_f8f6f4 v[118:121], v[2:9], v[50:57], v[118:121]
	v_mfma_f32_16x16x128_f8f6f4 v[114:117], v[10:17], v[50:57], v[114:117]
	s_waitcnt lgkmcnt(0)
	v_mfma_f32_16x16x128_f8f6f4 v[102:105], v[2:9], v[58:65], v[102:105]
	v_mfma_f32_16x16x128_f8f6f4 v[98:101], v[10:17], v[58:65], v[98:101]
	v_mfma_f32_16x16x128_f8f6f4 v[158:161], v[18:25], v[34:41], v[158:161]
	v_mfma_f32_16x16x128_f8f6f4 v[154:157], v[26:33], v[34:41], v[154:157]
	v_mfma_f32_16x16x128_f8f6f4 v[142:145], v[18:25], v[42:49], v[142:145]
	v_mfma_f32_16x16x128_f8f6f4 v[138:141], v[26:33], v[42:49], v[138:141]
	v_mfma_f32_16x16x128_f8f6f4 v[126:129], v[18:25], v[50:57], v[126:129]
	v_mfma_f32_16x16x128_f8f6f4 v[122:125], v[26:33], v[50:57], v[122:125]
	v_mfma_f32_16x16x128_f8f6f4 v[110:113], v[18:25], v[58:65], v[110:113]
	v_mfma_f32_16x16x128_f8f6f4 v[106:109], v[26:33], v[58:65], v[106:109]
	s_setprio 0
	s_barrier
	ds_read_b128 v[42:45], v169 offset:49152
	ds_read_b128 v[46:49], v169 offset:50176
	ds_read_b128 v[58:61], v169 offset:51200
	ds_read_b128 v[62:65], v169 offset:52224
	ds_read_b128 v[170:173], v169 offset:53248
	ds_read_b128 v[174:177], v169 offset:54272
	ds_read_b128 v[178:181], v169 offset:55296
	ds_read_b128 v[182:185], v169 offset:56320
	s_add_i32 s38, s74, 0x18000
	s_mov_b32 m0, s38
	s_nop 0
	global_load_lds_dwordx4 v166, s[36:37]
	s_add_i32 s38, s74, 0x1a000
	s_mov_b32 m0, s38
	s_nop 0
	global_load_lds_dwordx4 v167, s[36:37]
	s_add_i32 s34, s74, 0x8000
	s_mov_b32 m0, s34
	s_nop 0
	global_load_lds_dwordx4 v164, s[30:31]
	s_add_i32 s74, s74, 0xa000
	s_mov_b32 m0, s74
	s_nop 0
	global_load_lds_dwordx4 v165, s[30:31]
	s_waitcnt vmcnt(6)
	s_waitcnt lgkmcnt(0)
	s_barrier
	s_setprio 1
	s_waitcnt lgkmcnt(6)
	v_mfma_f32_16x16x128_f8f6f4 v[86:89], v[2:9], v[42:49], v[86:89]
	v_mfma_f32_16x16x128_f8f6f4 v[82:85], v[10:17], v[42:49], v[82:85]
	s_waitcnt lgkmcnt(4)
	v_mfma_f32_16x16x128_f8f6f4 v[70:73], v[2:9], v[58:65], v[70:73]
	v_mfma_f32_16x16x128_f8f6f4 v[66:69], v[10:17], v[58:65], v[66:69]
	s_waitcnt lgkmcnt(2)
	v_mfma_f32_16x16x128_f8f6f4 v[54:57], v[2:9], v[170:177], v[202:205]
	v_mfma_f32_16x16x128_f8f6f4 v[50:53], v[10:17], v[170:177], v[206:209]
	s_waitcnt lgkmcnt(0)
	v_mfma_f32_16x16x128_f8f6f4 v[38:41], v[2:9], v[178:185], v[210:213]
	v_mfma_f32_16x16x128_f8f6f4 v[34:37], v[10:17], v[178:185], v[214:217]
	v_mfma_f32_16x16x128_f8f6f4 v[94:97], v[18:25], v[42:49], v[94:97]
	v_mfma_f32_16x16x128_f8f6f4 v[90:93], v[26:33], v[42:49], v[90:93]
	v_mfma_f32_16x16x128_f8f6f4 v[78:81], v[18:25], v[58:65], v[78:81]
	v_mfma_f32_16x16x128_f8f6f4 v[74:77], v[26:33], v[58:65], v[74:77]
	v_mfma_f32_16x16x128_f8f6f4 v[62:65], v[18:25], v[170:177], v[218:221]
	v_mfma_f32_16x16x128_f8f6f4 v[58:61], v[26:33], v[170:177], v[186:189]
	v_mfma_f32_16x16x128_f8f6f4 v[46:49], v[18:25], v[178:185], v[190:193]
	v_mfma_f32_16x16x128_f8f6f4 v[42:45], v[26:33], v[178:185], v[194:197]
	s_setprio 0
	s_barrier
	s_add_i32 s73, s73, 2
	s_add_u32 s25, s25, 0x100
	s_addc_u32 s71, s71, 0
	s_add_u32 s26, s26, 0x100
	s_addc_u32 s27, s27, 0
	s_cmp_gt_u32 s73, 5
	s_branch .LBB0_1063
